# speedup vs baseline: 1.0226x; 1.0076x over previous
.LBB1_3:
	s_load_dwordx8 s[4:11], s[0:1], 0x0
	v_lshrrev_b32_e32 v1, 6, v0
	v_mov_b32_e32 v3, 0
	v_lshl_or_b32 v2, s2, 2, v1
	v_lshlrev_b32_e32 v7, 12, v2
	s_waitcnt lgkmcnt(0)
	v_lshl_add_u64 v[4:5], v[2:3], 2, s[4:5]
	global_load_dword v6, v[4:5], off
	v_and_b32_e32 v8, 0x3ff000, v7
	v_and_b32_e32 v1, 63, v0
	v_mov_b32_e32 v9, v3
	v_lshlrev_b32_e32 v4, 4, v1
	v_mov_b32_e32 v5, v3
	v_lshl_add_u64 v[8:9], s[8:9], 0, v[8:9]
	v_lshl_add_u64 v[38:39], v[8:9], 0, v[4:5]
	s_mov_b32 s3, 0xf800000
	v_mov_b32_e32 v78, 0x260
	s_waitcnt vmcnt(0)
	v_ashrrev_i32_e32 v7, 31, v6
	v_lshlrev_b64 v[6:7], 12, v[6:7]
	v_lshl_add_u64 v[6:7], s[6:7], 0, v[6:7]
	v_lshl_add_u64 v[40:41], v[6:7], 0, v[4:5]
	global_load_dwordx4 v[6:9], v[40:41], off
	global_load_dwordx4 v[10:13], v[38:39], off
	global_load_dwordx4 v[14:17], v[38:39], off offset:1024
	global_load_dwordx4 v[18:21], v[40:41], off offset:1024
	global_load_dwordx4 v[22:25], v[40:41], off offset:2048
	global_load_dwordx4 v[26:29], v[38:39], off offset:2048
	global_load_dwordx4 v[30:33], v[38:39], off offset:3072
	global_load_dwordx4 v[34:37], v[40:41], off offset:3072
	v_mbcnt_lo_u32_b32 v38, -1, 0
	v_mbcnt_hi_u32_b32 v38, -1, v38
	v_and_b32_e32 v39, 64, v38
	v_xor_b32_e32 v40, 32, v38
	v_add_u32_e32 v39, 64, v39
	v_cmp_lt_i32_e32 vcc, v40, v39
	s_load_dwordx4 s[4:7], s[0:1], 0x20
	s_load_dwordx2 s[8:9], s[0:1], 0x30
	v_cndmask_b32_e32 v40, v38, v40, vcc
	v_lshlrev_b32_e32 v70, 2, v40
	s_waitcnt vmcnt(6)
	v_pk_add_f32 v[6:7], v[6:7], v[10:11]
	v_pk_add_f32 v[8:9], v[8:9], v[12:13]
	s_waitcnt vmcnt(4)
	v_pk_add_f32 v[10:11], v[18:19], v[14:15]
	v_pk_add_f32 v[12:13], v[20:21], v[16:17]
	s_waitcnt vmcnt(2)
	v_pk_add_f32 v[14:15], v[22:23], v[26:27]
	v_pk_add_f32 v[16:17], v[24:25], v[28:29]
	v_mov_b32_e32 v22, v6
	v_mov_b32_e32 v23, v8
	v_mov_b32_e32 v24, v7
	v_mov_b32_e32 v25, v9
	v_mov_b32_e32 v26, v10
	v_mov_b32_e32 v27, v12
	v_mov_b32_e32 v28, v11
	v_mov_b32_e32 v29, v13
	v_pk_add_f32 v[22:23], v[22:23], v[24:25]
	v_pk_add_f32 v[24:25], v[26:27], v[28:29]
	s_waitcnt vmcnt(0)
	v_pk_add_f32 v[18:19], v[34:35], v[30:31]
	v_pk_add_f32 v[20:21], v[36:37], v[32:33]
	v_pk_add_f32 v[30:31], v[14:15], v[14:15] op_sel:[0,1] op_sel_hi:[1,0]
	v_pk_add_f32 v[32:33], v[16:17], v[16:17] op_sel:[0,1] op_sel_hi:[1,0]
	v_add_f32_e32 v26, v22, v23
	v_pk_add_f32 v[22:23], v[24:25], v[24:25] op_sel:[0,1] op_sel_hi:[1,0]
	v_mov_b32_e32 v35, v18
	v_mov_b32_e32 v31, v20
	v_mov_b32_e32 v33, v21
	v_add_f32_e32 v34, 0, v26
	v_mov_b32_e32 v23, v19
	v_pk_add_f32 v[24:25], v[30:31], v[32:33]
	v_pk_add_f32 v[22:23], v[34:35], v[22:23]
	s_nop 0
	v_pk_add_f32 v[22:23], v[22:23], v[24:25]
	v_xor_b32_e32 v24, 16, v38
	v_add_f32_e32 v22, v22, v23
	ds_bpermute_b32 v23, v70, v22
	v_cmp_lt_i32_e32 vcc, v24, v39
	s_waitcnt lgkmcnt(0)
	v_add_f32_e32 v22, v22, v23
	v_cndmask_b32_e32 v24, v38, v24, vcc
	v_lshlrev_b32_e32 v71, 2, v24
	ds_bpermute_b32 v23, v71, v22
	v_xor_b32_e32 v24, 8, v38
	v_cmp_lt_i32_e32 vcc, v24, v39
	s_waitcnt lgkmcnt(0)
	v_add_f32_e32 v22, v22, v23
	v_cndmask_b32_e32 v24, v38, v24, vcc
	v_lshlrev_b32_e32 v72, 2, v24
	v_xor_b32_e32 v24, 4, v38
	v_cmp_lt_i32_e32 vcc, v24, v39
	s_waitcnt lgkmcnt(0)
	s_nop 1
	v_add_f32_dpp v22, v22, v22 row_ror:8 row_mask:0xf bank_mask:0xf
	v_cndmask_b32_e32 v24, v38, v24, vcc
	v_lshlrev_b32_e32 v73, 2, v24
	v_xor_b32_e32 v24, 2, v38
	v_cmp_lt_i32_e32 vcc, v24, v39
	s_waitcnt lgkmcnt(0)
	s_nop 1
	v_add_f32_dpp v22, v22, v22 row_ror:4 row_mask:0xf bank_mask:0xf
	v_cndmask_b32_e32 v24, v38, v24, vcc
	v_lshlrev_b32_e32 v74, 2, v24
	v_xor_b32_e32 v24, 1, v38
	v_cmp_lt_i32_e32 vcc, v24, v39
	s_nop 1
	v_cndmask_b32_e32 v24, v38, v24, vcc
	v_lshlrev_b32_e32 v75, 2, v24
	s_waitcnt lgkmcnt(0)
	s_nop 1
	v_add_f32_dpp v38, v22, v22 row_ror:2 row_mask:0xf bank_mask:0xf
	global_load_dwordx4 v[22:25], v4, s[4:5]
	global_load_dwordx4 v[26:29], v4, s[6:7]
	global_load_dwordx4 v[30:33], v4, s[4:5] offset:1024
	global_load_dwordx4 v[34:37], v4, s[6:7] offset:1024
	s_waitcnt lgkmcnt(0)
	s_nop 1
	v_add_f32_dpp v38, v38, v38 row_ror:1 row_mask:0xf bank_mask:0xf
	v_mul_f32_e32 v38, 0x3a800000, v38
	v_pk_add_f32 v[54:55], v[6:7], v[38:39] op_sel_hi:[1,0] neg_lo:[0,1] neg_hi:[0,1]
	v_pk_add_f32 v[56:57], v[8:9], v[38:39] op_sel_hi:[1,0] neg_lo:[0,1] neg_hi:[0,1]
	v_pk_add_f32 v[58:59], v[10:11], v[38:39] op_sel_hi:[1,0] neg_lo:[0,1] neg_hi:[0,1]
	v_pk_add_f32 v[60:61], v[12:13], v[38:39] op_sel_hi:[1,0] neg_lo:[0,1] neg_hi:[0,1]
	v_mov_b32_e32 v40, v55
	v_mov_b32_e32 v41, v57
	v_mov_b32_e32 v44, v59
	v_mov_b32_e32 v45, v61
	v_pk_add_f32 v[62:63], v[14:15], v[38:39] op_sel_hi:[1,0] neg_lo:[0,1] neg_hi:[0,1]
	v_pk_add_f32 v[64:65], v[16:17], v[38:39] op_sel_hi:[1,0] neg_lo:[0,1] neg_hi:[0,1]
	v_pk_add_f32 v[66:67], v[18:19], v[38:39] op_sel_hi:[1,0] neg_lo:[0,1] neg_hi:[0,1]
	v_pk_add_f32 v[68:69], v[20:21], v[38:39] op_sel_hi:[1,0] neg_lo:[0,1] neg_hi:[0,1]
	v_mov_b32_e32 v38, v54
	v_mov_b32_e32 v39, v56
	v_mov_b32_e32 v42, v58
	v_mov_b32_e32 v43, v60
	v_pk_mul_f32 v[40:41], v[40:41], v[40:41]
	v_pk_mul_f32 v[44:45], v[44:45], v[44:45]
	v_mul_f32_e32 v46, v62, v62
	v_mul_f32_e32 v48, v64, v64
	v_pk_fma_f32 v[38:39], v[38:39], v[38:39], v[40:41]
	v_pk_fma_f32 v[40:41], v[42:43], v[42:43], v[44:45]
	v_pk_mul_f32 v[50:51], v[66:67], v[66:67]
	v_pk_mul_f32 v[52:53], v[68:69], v[68:69]
	v_pk_fma_f32 v[46:47], v[62:63], v[62:63], v[46:47] op_sel_hi:[1,1,0]
	v_pk_fma_f32 v[48:49], v[64:65], v[64:65], v[48:49] op_sel_hi:[1,1,0]
	v_pk_add_f32 v[38:39], v[38:39], v[38:39] op_sel_hi:[0,1]
	v_pk_add_f32 v[40:41], v[40:41], v[40:41] op_sel_hi:[0,1]
	v_mov_b32_e32 v46, v50
	v_mov_b32_e32 v48, v51
	v_mov_b32_e32 v38, v52
	v_mov_b32_e32 v40, v53
	v_pk_add_f32 v[42:43], v[46:47], v[48:49]
	v_pk_add_f32 v[38:39], v[38:39], v[40:41]
	s_nop 0
	v_pk_add_f32 v[38:39], v[42:43], v[38:39]
	s_nop 0
	v_add_f32_e32 v76, v38, v39
	global_load_dwordx4 v[38:41], v4, s[4:5] offset:2048
	global_load_dwordx4 v[42:45], v4, s[6:7] offset:2048
	global_load_dwordx4 v[46:49], v4, s[4:5] offset:3072
	global_load_dwordx4 v[50:53], v4, s[6:7] offset:3072
	ds_bpermute_b32 v70, v70, v76
	s_waitcnt lgkmcnt(0)
	v_add_f32_e32 v70, v76, v70
	ds_bpermute_b32 v71, v71, v70
	v_mov_b32_e32 v76, 0x3727c5ac
	s_waitcnt lgkmcnt(0)
	v_add_f32_e32 v70, v70, v71
	s_waitcnt lgkmcnt(0)
	s_nop 1
	v_add_f32_dpp v70, v70, v70 row_ror:8 row_mask:0xf bank_mask:0xf
	v_lshlrev_b64 v[72:73], 11, v[2:3]
	v_lshl_add_u64 v[72:73], s[8:9], 0, v[72:73]
	s_waitcnt lgkmcnt(0)
	s_nop 1
	v_add_f32_dpp v77, v70, v70 row_ror:4 row_mask:0xf bank_mask:0xf
	v_lshlrev_b64 v[70:71], 12, v[2:3]
	v_lshlrev_b32_e32 v2, 3, v1
	v_lshl_add_u64 v[70:71], s[10:11], 0, v[70:71]
	v_lshl_add_u64 v[4:5], v[70:71], 0, v[4:5]
	s_waitcnt lgkmcnt(0)
	s_nop 1
	v_add_f32_dpp v74, v77, v77 row_ror:2 row_mask:0xf bank_mask:0xf
	global_store_dwordx4 v[4:5], v[6:9], off
	global_store_dwordx4 v[4:5], v[10:13], off offset:1024
	global_store_dwordx4 v[4:5], v[14:17], off offset:2048
	global_store_dwordx4 v[4:5], v[18:21], off offset:3072
	v_lshl_add_u64 v[2:3], v[72:73], 0, v[2:3]
	s_waitcnt lgkmcnt(0)
	s_nop 1
	v_add_f32_dpp v1, v74, v74 row_ror:1 row_mask:0xf bank_mask:0xf
	v_fmac_f32_e32 v76, 0x3a800000, v1
	v_mul_f32_e32 v1, 0x4f800000, v76
	v_cmp_gt_f32_e32 vcc, s3, v76
	s_nop 1
	v_cndmask_b32_e32 v1, v76, v1, vcc
	v_sqrt_f32_e32 v70, v1
	s_nop 0
	v_add_u32_e32 v6, -1, v70
	v_add_u32_e32 v7, 1, v70
	v_fma_f32 v8, -v6, v70, v1
	v_fma_f32 v9, -v7, v70, v1
	v_cmp_ge_f32_e64 s[4:5], 0, v8
	s_nop 1
	v_cndmask_b32_e64 v6, v70, v6, s[4:5]
	v_cmp_lt_f32_e64 s[4:5], 0, v9
	s_nop 1
	v_cndmask_b32_e64 v6, v6, v7, s[4:5]
	v_mul_f32_e32 v7, 0x37800000, v6
	v_cndmask_b32_e32 v6, v6, v7, vcc
	v_cmp_class_f32_e32 vcc, v1, v78
	s_nop 1
	v_cndmask_b32_e32 v1, v6, v1, vcc
	v_div_scale_f32 v6, s[4:5], v1, v1, 1.0
	v_rcp_f32_e32 v7, v6
	v_div_scale_f32 v4, vcc, 1.0, v1, 1.0
	v_fma_f32 v5, -v6, v7, 1.0
	v_fmac_f32_e32 v7, v5, v7
	v_mul_f32_e32 v5, v4, v7
	v_fma_f32 v8, -v6, v5, v4
	v_fmac_f32_e32 v5, v8, v7
	v_fma_f32 v4, -v6, v5, v4
	v_div_fmas_f32 v4, v4, v7, v5
	v_div_fixup_f32 v4, v4, v1, 1.0
	v_pk_mul_f32 v[6:7], v[54:55], v[4:5] op_sel_hi:[1,0]
	v_pk_mul_f32 v[8:9], v[56:57], v[4:5] op_sel_hi:[1,0]
	v_pk_mul_f32 v[10:11], v[58:59], v[4:5] op_sel_hi:[1,0]
	v_pk_mul_f32 v[12:13], v[60:61], v[4:5] op_sel_hi:[1,0]
	v_pk_mul_f32 v[14:15], v[62:63], v[4:5] op_sel_hi:[1,0]
	v_pk_mul_f32 v[16:17], v[64:65], v[4:5] op_sel_hi:[1,0]
	v_pk_mul_f32 v[18:19], v[66:67], v[4:5] op_sel_hi:[1,0]
	v_pk_mul_f32 v[4:5], v[68:69], v[4:5] op_sel_hi:[1,0]
	s_waitcnt vmcnt(10)
	v_pk_fma_f32 v[6:7], v[22:23], v[6:7], v[26:27]
	v_pk_fma_f32 v[8:9], v[24:25], v[8:9], v[28:29]
	s_waitcnt vmcnt(8)
	v_pk_fma_f32 v[10:11], v[30:31], v[10:11], v[34:35]
	v_pk_fma_f32 v[12:13], v[32:33], v[12:13], v[36:37]
	s_waitcnt vmcnt(6)
	v_pk_fma_f32 v[14:15], v[14:15], v[38:39], v[42:43]
	v_pk_fma_f32 v[16:17], v[16:17], v[40:41], v[44:45]
	s_waitcnt vmcnt(4)
	v_pk_fma_f32 v[18:19], v[18:19], v[46:47], v[50:51]
	v_pk_fma_f32 v[4:5], v[4:5], v[48:49], v[52:53]
	v_cvt_pk_f16_f32 v6, v6, v7
	v_cvt_pk_f16_f32 v7, v8, v9
	v_cvt_pk_f16_f32 v8, v10, v11
	v_cvt_pk_f16_f32 v9, v12, v13
	v_cvt_pk_f16_f32 v10, v14, v15
	v_cvt_pk_f16_f32 v11, v16, v17
	v_cvt_pk_f16_f32 v12, v18, v19
	v_cvt_pk_f16_f32 v13, v4, v5
	global_store_dwordx2 v[2:3], v[6:7], off
	global_store_dwordx2 v[2:3], v[8:9], off offset:512
	global_store_dwordx2 v[2:3], v[10:11], off offset:1024
	global_store_dwordx2 v[2:3], v[12:13], off offset:1536
	s_cbranch_execnz .LBB1_2

_Z9ln_kernelILi2EEvPKiPKfS3_PfS3_S3_PDF16_:
	s_load_dwordx8 s[4:11], s[0:1], 0x8
	v_and_b32_e32 v12, 63, v0
	v_lshrrev_b32_e32 v0, 6, v0
	v_lshl_or_b32 v6, s2, 2, v0
	v_ashrrev_i32_e32 v7, 31, v6
	v_lshlrev_b64 v[2:3], 11, v[6:7]
	v_mov_b32_e32 v1, 0
	s_waitcnt lgkmcnt(0)
	v_lshl_add_u64 v[8:9], s[4:5], 0, v[2:3]
	v_lshlrev_b32_e32 v4, 3, v12
	v_mov_b32_e32 v5, v1
	v_lshl_add_u64 v[8:9], v[8:9], 0, v[4:5]
	s_mov_b64 s[2:3], 0x400000
	v_lshl_add_u64 v[10:11], v[8:9], 0, s[2:3]
	s_mov_b32 s2, 0x400000
	global_load_dwordx2 v[16:17], v[8:9], off
	global_load_dwordx2 v[18:19], v[8:9], off offset:512
	global_load_dwordx2 v[20:21], v[8:9], off offset:1024
	global_load_dwordx2 v[22:23], v[8:9], off offset:1536
	v_add_co_u32_e32 v8, vcc, s2, v8
	global_load_dwordx2 v[24:25], v[10:11], off offset:512
	global_load_dwordx2 v[26:27], v[10:11], off offset:1024
	global_load_dwordx2 v[28:29], v[10:11], off offset:1536
	v_addc_co_u32_e32 v9, vcc, 0, v9, vcc
	global_load_dwordx2 v[30:31], v[8:9], off
	v_lshlrev_b64 v[6:7], 12, v[6:7]
	v_lshlrev_b32_e32 v0, 4, v12
	v_lshl_add_u64 v[6:7], s[8:9], 0, v[6:7]
	v_lshl_add_u64 v[6:7], v[6:7], 0, v[0:1]
	global_load_dwordx4 v[8:11], v[6:7], off offset:1024
	global_load_dwordx4 v[12:15], v0, s[6:7] offset:1024
	s_waitcnt vmcnt(9)
	v_cvt_f32_f16_e32 v32, v16
	s_waitcnt vmcnt(8)
	v_cvt_f32_f16_e32 v36, v18
	v_cvt_f32_f16_sdwa v37, v18 dst_sel:DWORD dst_unused:UNUSED_PAD src0_sel:WORD_1
	v_cvt_f32_f16_e32 v38, v19
	v_cvt_f32_f16_sdwa v39, v19 dst_sel:DWORD dst_unused:UNUSED_PAD src0_sel:WORD_1
	s_waitcnt vmcnt(7)
	v_cvt_f32_f16_e32 v40, v20
	v_cvt_f32_f16_sdwa v41, v20 dst_sel:DWORD dst_unused:UNUSED_PAD src0_sel:WORD_1
	v_cvt_f32_f16_e32 v42, v21
	v_cvt_f32_f16_sdwa v43, v21 dst_sel:DWORD dst_unused:UNUSED_PAD src0_sel:WORD_1
	s_waitcnt vmcnt(6)
	v_cvt_f32_f16_e32 v44, v22
	v_cvt_f32_f16_sdwa v45, v22 dst_sel:DWORD dst_unused:UNUSED_PAD src0_sel:WORD_1
	v_cvt_f32_f16_e32 v46, v23
	v_cvt_f32_f16_sdwa v47, v23 dst_sel:DWORD dst_unused:UNUSED_PAD src0_sel:WORD_1
	s_waitcnt vmcnt(5)
	v_cvt_f32_f16_e32 v20, v24
	v_cvt_f32_f16_sdwa v21, v24 dst_sel:DWORD dst_unused:UNUSED_PAD src0_sel:WORD_1
	v_cvt_f32_f16_e32 v22, v25
	v_cvt_f32_f16_sdwa v23, v25 dst_sel:DWORD dst_unused:UNUSED_PAD src0_sel:WORD_1
	s_waitcnt vmcnt(4)
	v_cvt_f32_f16_e32 v24, v26
	v_cvt_f32_f16_sdwa v25, v26 dst_sel:DWORD dst_unused:UNUSED_PAD src0_sel:WORD_1
	v_cvt_f32_f16_e32 v26, v27
	v_cvt_f32_f16_sdwa v27, v27 dst_sel:DWORD dst_unused:UNUSED_PAD src0_sel:WORD_1
	s_waitcnt vmcnt(3)
	v_cvt_f32_f16_e32 v48, v28
	v_cvt_f32_f16_sdwa v49, v28 dst_sel:DWORD dst_unused:UNUSED_PAD src0_sel:WORD_1
	v_cvt_f32_f16_e32 v28, v29
	v_cvt_f32_f16_sdwa v29, v29 dst_sel:DWORD dst_unused:UNUSED_PAD src0_sel:WORD_1
	v_cvt_f32_f16_sdwa v33, v16 dst_sel:DWORD dst_unused:UNUSED_PAD src0_sel:WORD_1
	v_cvt_f32_f16_e32 v34, v17
	v_cvt_f32_f16_sdwa v35, v17 dst_sel:DWORD dst_unused:UNUSED_PAD src0_sel:WORD_1
	s_waitcnt vmcnt(2)
	v_cvt_f32_f16_e32 v50, v30
	v_cvt_f32_f16_sdwa v51, v30 dst_sel:DWORD dst_unused:UNUSED_PAD src0_sel:WORD_1
	v_cvt_f32_f16_e32 v52, v31
	v_cvt_f32_f16_sdwa v53, v31 dst_sel:DWORD dst_unused:UNUSED_PAD src0_sel:WORD_1
	global_load_dwordx4 v[16:19], v[6:7], off
	v_pk_add_f32 v[36:37], v[36:37], v[20:21]
	v_pk_add_f32 v[38:39], v[38:39], v[22:23]
	global_load_dwordx4 v[20:23], v[6:7], off offset:2048
	v_pk_add_f32 v[40:41], v[40:41], v[24:25]
	v_pk_add_f32 v[42:43], v[42:43], v[26:27]
	global_load_dwordx4 v[24:27], v[6:7], off offset:3072
	v_pk_add_f32 v[46:47], v[46:47], v[28:29]
	global_load_dwordx4 v[28:31], v0, s[6:7] offset:2048
	s_waitcnt vmcnt(5)
	v_pk_add_f32 v[36:37], v[8:9], v[36:37]
	v_pk_add_f32 v[38:39], v[10:11], v[38:39]
	global_load_dwordx4 v[8:11], v0, s[6:7]
	v_pk_add_f32 v[44:45], v[44:45], v[48:49]
	v_pk_add_f32 v[48:49], v[32:33], v[50:51]
	v_pk_add_f32 v[50:51], v[34:35], v[52:53]
	global_load_dwordx4 v[32:35], v0, s[6:7] offset:3072
	s_waitcnt vmcnt(6)
	v_pk_add_f32 v[12:13], v[12:13], v[36:37]
	v_pk_add_f32 v[14:15], v[14:15], v[38:39]
	s_load_dwordx4 s[4:7], s[0:1], 0x28
	s_mov_b32 s0, 0xf800000
	s_waitcnt lgkmcnt(0)
	v_lshl_add_u64 v[2:3], s[6:7], 0, v[2:3]
	s_waitcnt vmcnt(4)
	v_pk_add_f32 v[20:21], v[20:21], v[40:41]
	v_pk_add_f32 v[22:23], v[22:23], v[42:43]
	v_pk_add_f32 v[40:41], v[16:17], v[48:49]
	v_pk_add_f32 v[42:43], v[18:19], v[50:51]
	s_waitcnt vmcnt(3)
	v_pk_add_f32 v[24:25], v[24:25], v[44:45]
	v_pk_add_f32 v[26:27], v[26:27], v[46:47]
	s_waitcnt vmcnt(2)
	v_pk_add_f32 v[16:17], v[28:29], v[20:21]
	v_pk_add_f32 v[18:19], v[30:31], v[22:23]
	s_waitcnt vmcnt(1)
	v_pk_add_f32 v[8:9], v[8:9], v[40:41]
	v_pk_add_f32 v[10:11], v[10:11], v[42:43]
	v_mov_b32_e32 v28, v13
	v_mov_b32_e32 v29, v15
	s_waitcnt vmcnt(0)
	v_pk_add_f32 v[20:21], v[32:33], v[24:25]
	v_pk_add_f32 v[22:23], v[34:35], v[26:27]
	v_mov_b32_e32 v24, v8
	v_mov_b32_e32 v25, v10
	v_mov_b32_e32 v26, v9
	v_mov_b32_e32 v27, v11
	v_pk_add_f32 v[24:25], v[24:25], v[26:27]
	v_mov_b32_e32 v26, v12
	v_mov_b32_e32 v27, v14
	v_pk_add_f32 v[26:27], v[26:27], v[28:29]
	v_add_f32_e32 v1, v24, v25
	v_pk_add_f32 v[26:27], v[26:27], v[26:27] op_sel:[0,1] op_sel_hi:[1,0]
	v_pk_add_f32 v[28:29], v[16:17], v[16:17] op_sel:[0,1] op_sel_hi:[1,0]
	v_pk_add_f32 v[30:31], v[18:19], v[18:19] op_sel:[0,1] op_sel_hi:[1,0]
	v_add_f32_e32 v24, 0, v1
	v_mov_b32_e32 v25, v20
	v_mov_b32_e32 v27, v21
	v_mov_b32_e32 v29, v22
	v_mov_b32_e32 v31, v23
	v_pk_add_f32 v[24:25], v[24:25], v[26:27]
	v_pk_add_f32 v[26:27], v[28:29], v[30:31]
	s_nop 0
	v_pk_add_f32 v[24:25], v[24:25], v[26:27]
	s_nop 0
	v_add_f32_e32 v1, v24, v25
	v_mbcnt_lo_u32_b32 v24, -1, 0
	v_mbcnt_hi_u32_b32 v24, -1, v24
	v_and_b32_e32 v25, 64, v24
	v_add_u32_e32 v25, 64, v25
	v_xor_b32_e32 v26, 32, v24
	v_cmp_lt_i32_e32 vcc, v26, v25
	s_nop 1
	v_cndmask_b32_e32 v26, v24, v26, vcc
	v_lshlrev_b32_e32 v52, 2, v26
	ds_bpermute_b32 v26, v52, v1
	s_waitcnt lgkmcnt(0)
	v_add_f32_e32 v1, v1, v26
	v_xor_b32_e32 v26, 16, v24
	v_cmp_lt_i32_e32 vcc, v26, v25
	s_nop 1
	v_cndmask_b32_e32 v26, v24, v26, vcc
	v_lshlrev_b32_e32 v53, 2, v26
	ds_bpermute_b32 v26, v53, v1
	s_waitcnt lgkmcnt(0)
	v_add_f32_e32 v1, v1, v26
	v_xor_b32_e32 v26, 8, v24
	v_cmp_lt_i32_e32 vcc, v26, v25
	s_nop 1
	v_cndmask_b32_e32 v26, v24, v26, vcc
	v_lshlrev_b32_e32 v54, 2, v26
	s_waitcnt lgkmcnt(0)
	s_nop 1
	v_add_f32_dpp v1, v1, v1 row_ror:8 row_mask:0xf bank_mask:0xf
	v_xor_b32_e32 v26, 4, v24
	v_cmp_lt_i32_e32 vcc, v26, v25
	s_nop 1
	v_cndmask_b32_e32 v26, v24, v26, vcc
	v_lshlrev_b32_e32 v55, 2, v26
	s_waitcnt lgkmcnt(0)
	s_nop 1
	v_add_f32_dpp v1, v1, v1 row_ror:4 row_mask:0xf bank_mask:0xf
	v_xor_b32_e32 v26, 2, v24
	v_cmp_lt_i32_e32 vcc, v26, v25
	s_nop 1
	v_cndmask_b32_e32 v26, v24, v26, vcc
	v_lshlrev_b32_e32 v56, 2, v26
	s_waitcnt lgkmcnt(0)
	s_nop 1
	v_add_f32_dpp v1, v1, v1 row_ror:2 row_mask:0xf bank_mask:0xf
	v_xor_b32_e32 v26, 1, v24
	v_cmp_lt_i32_e32 vcc, v26, v25
	s_nop 1
	v_cndmask_b32_e32 v24, v24, v26, vcc
	v_lshlrev_b32_e32 v57, 2, v24
	s_waitcnt lgkmcnt(0)
	s_nop 1
	v_add_f32_dpp v1, v1, v1 row_ror:1 row_mask:0xf bank_mask:0xf
	v_mul_f32_e32 v24, 0x3a800000, v1
	v_pk_add_f32 v[36:37], v[8:9], v[24:25] op_sel_hi:[1,0] neg_lo:[0,1] neg_hi:[0,1]
	v_pk_add_f32 v[38:39], v[10:11], v[24:25] op_sel_hi:[1,0] neg_lo:[0,1] neg_hi:[0,1]
	v_mov_b32_e32 v28, v37
	v_mov_b32_e32 v29, v39
	v_pk_add_f32 v[40:41], v[12:13], v[24:25] op_sel_hi:[1,0] neg_lo:[0,1] neg_hi:[0,1]
	v_pk_add_f32 v[42:43], v[14:15], v[24:25] op_sel_hi:[1,0] neg_lo:[0,1] neg_hi:[0,1]
	v_mov_b32_e32 v26, v36
	v_mov_b32_e32 v27, v38
	v_pk_mul_f32 v[28:29], v[28:29], v[28:29]
	v_mov_b32_e32 v30, v41
	v_mov_b32_e32 v31, v43
	v_pk_fma_f32 v[26:27], v[26:27], v[26:27], v[28:29]
	v_mov_b32_e32 v28, v40
	v_mov_b32_e32 v29, v42
	v_pk_mul_f32 v[30:31], v[30:31], v[30:31]
	v_pk_add_f32 v[44:45], v[16:17], v[24:25] op_sel_hi:[1,0] neg_lo:[0,1] neg_hi:[0,1]
	v_pk_fma_f32 v[28:29], v[28:29], v[28:29], v[30:31]
	v_mul_f32_e32 v30, v44, v44
	v_pk_fma_f32 v[30:31], v[44:45], v[44:45], v[30:31] op_sel_hi:[1,1,0]
	v_pk_add_f32 v[46:47], v[18:19], v[24:25] op_sel_hi:[1,0] neg_lo:[0,1] neg_hi:[0,1]
	v_pk_add_f32 v[48:49], v[20:21], v[24:25] op_sel_hi:[1,0] neg_lo:[0,1] neg_hi:[0,1]
	v_mul_f32_e32 v30, v46, v46
	v_pk_add_f32 v[50:51], v[22:23], v[24:25] op_sel_hi:[1,0] neg_lo:[0,1] neg_hi:[0,1]
	v_pk_fma_f32 v[32:33], v[46:47], v[46:47], v[30:31] op_sel_hi:[1,1,0]
	v_pk_mul_f32 v[34:35], v[48:49], v[48:49]
	v_pk_add_f32 v[26:27], v[26:27], v[26:27] op_sel_hi:[0,1]
	v_pk_add_f32 v[28:29], v[28:29], v[28:29] op_sel_hi:[0,1]
	v_pk_mul_f32 v[24:25], v[50:51], v[50:51]
	v_mov_b32_e32 v30, v34
	v_mov_b32_e32 v32, v35
	v_mov_b32_e32 v26, v24
	v_mov_b32_e32 v28, v25
	v_pk_add_f32 v[30:31], v[30:31], v[32:33]
	v_pk_add_f32 v[24:25], v[26:27], v[28:29]
	s_nop 0
	v_pk_add_f32 v[24:25], v[30:31], v[24:25]
	s_nop 0
	v_add_f32_e32 v1, v24, v25
	ds_bpermute_b32 v24, v52, v1
	s_waitcnt lgkmcnt(0)
	v_add_f32_e32 v1, v1, v24
	ds_bpermute_b32 v24, v53, v1
	s_waitcnt lgkmcnt(0)
	v_add_f32_e32 v1, v1, v24
	s_waitcnt lgkmcnt(0)
	s_nop 1
	v_add_f32_dpp v1, v1, v1 row_ror:8 row_mask:0xf bank_mask:0xf
	s_waitcnt lgkmcnt(0)
	s_nop 1
	v_add_f32_dpp v1, v1, v1 row_ror:4 row_mask:0xf bank_mask:0xf
	global_load_dwordx4 v[24:27], v0, s[10:11]
	global_load_dwordx4 v[28:31], v0, s[10:11] offset:1024
	s_waitcnt lgkmcnt(0)
	s_nop 1
	v_add_f32_dpp v1, v1, v1 row_ror:2 row_mask:0xf bank_mask:0xf
	global_store_dwordx4 v[6:7], v[8:11], off
	global_store_dwordx4 v[6:7], v[12:15], off offset:1024
	global_store_dwordx4 v[6:7], v[16:19], off offset:2048
	global_store_dwordx4 v[6:7], v[20:23], off offset:3072
	s_waitcnt lgkmcnt(0)
	s_nop 1
	v_add_f32_dpp v1, v1, v1 row_ror:1 row_mask:0xf bank_mask:0xf
	v_mov_b32_e32 v32, 0x3727c5ac
	v_fmac_f32_e32 v32, 0x3a800000, v1
	v_mul_f32_e32 v1, 0x4f800000, v32
	v_cmp_gt_f32_e32 vcc, s0, v32
	global_load_dwordx4 v[12:15], v0, s[4:5]
	global_load_dwordx4 v[16:19], v0, s[4:5] offset:1024
	v_cndmask_b32_e32 v1, v32, v1, vcc
	v_sqrt_f32_e32 v32, v1
	global_load_dwordx4 v[8:11], v0, s[10:11] offset:2048
	v_add_u32_e32 v6, -1, v32
	v_fma_f32 v7, -v6, v32, v1
	v_cmp_ge_f32_e64 s[0:1], 0, v7
	v_add_u32_e32 v7, 1, v32
	v_fma_f32 v20, -v7, v32, v1
	v_cndmask_b32_e64 v6, v32, v6, s[0:1]
	v_cmp_lt_f32_e64 s[0:1], 0, v20
	global_load_dwordx4 v[20:23], v0, s[4:5] offset:2048
	s_nop 0
	v_cndmask_b32_e64 v6, v6, v7, s[0:1]
	v_mul_f32_e32 v7, 0x37800000, v6
	v_cndmask_b32_e32 v6, v6, v7, vcc
	v_mov_b32_e32 v7, 0x260
	v_cmp_class_f32_e32 vcc, v1, v7
	s_nop 1
	v_cndmask_b32_e32 v1, v6, v1, vcc
	v_div_scale_f32 v32, s[0:1], v1, v1, 1.0
	v_rcp_f32_e32 v33, v32
	v_lshl_add_u64 v[6:7], v[2:3], 0, v[4:5]
	v_div_scale_f32 v34, vcc, 1.0, v1, 1.0
	v_fma_f32 v2, -v32, v33, 1.0
	v_fmac_f32_e32 v33, v2, v33
	v_mul_f32_e32 v35, v34, v33
	v_fma_f32 v2, -v32, v35, v34
	v_fmac_f32_e32 v35, v2, v33
	v_fma_f32 v32, -v32, v35, v34
	global_load_dwordx4 v[2:5], v0, s[10:11] offset:3072
	v_div_fmas_f32 v52, v32, v33, v35
	global_load_dwordx4 v[32:35], v0, s[4:5] offset:3072
	v_div_fixup_f32 v0, v52, v1, 1.0
	v_pk_mul_f32 v[36:37], v[36:37], v[0:1] op_sel_hi:[1,0]
	s_waitcnt vmcnt(5)
	v_pk_fma_f32 v[12:13], v[24:25], v[36:37], v[12:13]
	v_pk_mul_f32 v[24:25], v[38:39], v[0:1] op_sel_hi:[1,0]
	v_cvt_pk_f16_f32 v12, v12, v13
	v_pk_fma_f32 v[14:15], v[26:27], v[24:25], v[14:15]
	s_nop 0
	v_cvt_pk_f16_f32 v13, v14, v15
	global_store_dwordx2 v[6:7], v[12:13], off
	v_pk_mul_f32 v[12:13], v[40:41], v[0:1] op_sel_hi:[1,0]
	v_pk_mul_f32 v[14:15], v[42:43], v[0:1] op_sel_hi:[1,0]
	s_waitcnt vmcnt(5)
	v_pk_fma_f32 v[12:13], v[28:29], v[12:13], v[16:17]
	v_pk_fma_f32 v[14:15], v[30:31], v[14:15], v[18:19]
	v_cvt_pk_f16_f32 v12, v12, v13
	v_cvt_pk_f16_f32 v13, v14, v15
	global_store_dwordx2 v[6:7], v[12:13], off offset:512
	v_pk_mul_f32 v[12:13], v[44:45], v[0:1] op_sel_hi:[1,0]
	s_waitcnt vmcnt(4)
	v_pk_fma_f32 v[8:9], v[12:13], v[8:9], v[20:21]
	v_pk_mul_f32 v[12:13], v[46:47], v[0:1] op_sel_hi:[1,0]
	v_cvt_pk_f16_f32 v8, v8, v9
	v_pk_fma_f32 v[10:11], v[12:13], v[10:11], v[22:23]
	s_nop 0
	v_cvt_pk_f16_f32 v9, v10, v11
	global_store_dwordx2 v[6:7], v[8:9], off offset:1024
	v_pk_mul_f32 v[8:9], v[48:49], v[0:1] op_sel_hi:[1,0]
	v_pk_mul_f32 v[0:1], v[50:51], v[0:1] op_sel_hi:[1,0]
	s_waitcnt vmcnt(3)
	v_pk_fma_f32 v[2:3], v[8:9], v[2:3], v[32:33]
	v_pk_fma_f32 v[0:1], v[0:1], v[4:5], v[34:35]
	v_cvt_pk_f16_f32 v2, v2, v3
	v_cvt_pk_f16_f32 v3, v0, v1
	global_store_dwordx2 v[6:7], v[2:3], off offset:1536
	s_endpgm
	s_endpgm
	s_endpgm
	s_endpgm
	s_endpgm
	s_endpgm
	s_endpgm
	s_endpgm
	s_endpgm
	s_endpgm
	s_endpgm
	s_endpgm
	s_endpgm
	s_endpgm

_Z9ln_kernelILi0EEvPKiPKfS3_PfS3_S3_PDF16_:
	s_load_dwordx8 s[4:11], s[0:1], 0x18
	v_and_b32_e32 v52, 63, v0
	v_lshrrev_b32_e32 v0, 6, v0
	v_lshl_or_b32 v0, s2, 2, v0
	v_ashrrev_i32_e32 v1, 31, v0
	v_lshlrev_b64 v[2:3], 12, v[0:1]
	s_waitcnt lgkmcnt(0)
	v_lshl_add_u64 v[4:5], s[4:5], 0, v[2:3]
	v_lshlrev_b32_e32 v2, 4, v52
	v_mov_b32_e32 v3, 0
	v_lshl_add_u64 v[20:21], v[4:5], 0, v[2:3]
	global_load_dwordx4 v[4:7], v[20:21], off offset:1024
	global_load_dwordx4 v[8:11], v[20:21], off offset:2048
	global_load_dwordx4 v[12:15], v[20:21], off
	global_load_dwordx4 v[16:19], v[20:21], off offset:3072
	v_mbcnt_lo_u32_b32 v20, -1, 0
	v_mbcnt_hi_u32_b32 v32, -1, v20
	v_and_b32_e32 v20, 64, v32
	v_xor_b32_e32 v21, 32, v32
	v_add_u32_e32 v34, 64, v20
	v_cmp_lt_i32_e32 vcc, v21, v34
	v_xor_b32_e32 v33, 16, v32
	s_mov_b32 s0, 0xf800000
	v_cndmask_b32_e32 v20, v32, v21, vcc
	v_lshlrev_b32_e32 v53, 2, v20
	v_cmp_lt_i32_e32 vcc, v33, v34
	v_lshlrev_b64 v[0:1], 11, v[0:1]
	v_lshl_add_u64 v[0:1], s[10:11], 0, v[0:1]
	s_waitcnt vmcnt(3)
	v_mov_b32_e32 v36, v5
	v_mov_b32_e32 v37, v6
	v_mov_b32_e32 v5, v7
	s_waitcnt vmcnt(1)
	v_mov_b32_e32 v22, v12
	v_mov_b32_e32 v23, v14
	v_mov_b32_e32 v24, v13
	v_mov_b32_e32 v25, v15
	v_mov_b32_e32 v6, v9
	v_mov_b32_e32 v20, v11
	s_waitcnt vmcnt(0)
	v_mov_b32_e32 v21, v16
	v_pk_add_f32 v[26:27], v[36:37], v[4:5]
	v_pk_add_f32 v[22:23], v[22:23], v[24:25]
	v_pk_add_f32 v[28:29], v[8:9], v[6:7]
	v_pk_add_f32 v[30:31], v[10:11], v[20:21]
	v_pk_add_f32 v[24:25], v[26:27], v[26:27] op_sel:[0,1] op_sel_hi:[1,0]
	v_add_f32_e32 v5, v22, v23
	v_mov_b32_e32 v29, v18
	v_mov_b32_e32 v31, v19
	v_add_f32_e32 v20, 0, v5
	v_mov_b32_e32 v25, v17
	v_pk_add_f32 v[22:23], v[28:29], v[30:31]
	v_pk_add_f32 v[20:21], v[20:21], v[24:25]
	v_pk_mov_b32 v[36:37], v[36:37], v[36:37] op_sel:[1,0]
	v_pk_add_f32 v[20:21], v[20:21], v[22:23]
	s_nop 0
	v_add_f32_e32 v5, v20, v21
	ds_bpermute_b32 v6, v53, v5
	v_cndmask_b32_e32 v21, v32, v33, vcc
	v_lshlrev_b32_e32 v54, 2, v21
	v_xor_b32_e32 v20, 8, v32
	v_cmp_lt_i32_e32 vcc, v20, v34
	s_waitcnt lgkmcnt(0)
	v_add_f32_e32 v5, v5, v6
	ds_bpermute_b32 v6, v54, v5
	v_cndmask_b32_e32 v20, v32, v20, vcc
	v_lshlrev_b32_e32 v55, 2, v20
	v_xor_b32_e32 v21, 4, v32
	v_cmp_lt_i32_e32 vcc, v21, v34
	s_waitcnt lgkmcnt(0)
	v_add_f32_e32 v5, v5, v6
	v_cndmask_b32_e32 v21, v32, v21, vcc
	v_lshlrev_b32_e32 v56, 2, v21
	v_xor_b32_e32 v20, 2, v32
	v_cmp_lt_i32_e32 vcc, v20, v34
	s_waitcnt lgkmcnt(0)
	s_nop 1
	v_add_f32_dpp v5, v5, v5 row_ror:8 row_mask:0xf bank_mask:0xf
	v_cndmask_b32_e32 v20, v32, v20, vcc
	v_lshlrev_b32_e32 v57, 2, v20
	v_xor_b32_e32 v21, 1, v32
	v_cmp_lt_i32_e32 vcc, v21, v34
	s_waitcnt lgkmcnt(0)
	s_nop 1
	v_add_f32_dpp v5, v5, v5 row_ror:4 row_mask:0xf bank_mask:0xf
	v_cndmask_b32_e32 v20, v32, v21, vcc
	v_lshlrev_b32_e32 v58, 2, v20
	global_load_dwordx4 v[20:23], v2, s[6:7]
	global_load_dwordx4 v[24:27], v2, s[8:9]
	global_load_dwordx4 v[28:31], v2, s[6:7] offset:1024
	global_load_dwordx4 v[32:35], v2, s[8:9] offset:1024
	s_waitcnt lgkmcnt(0)
	s_nop 1
	v_add_f32_dpp v6, v5, v5 row_ror:2 row_mask:0xf bank_mask:0xf
	v_mov_b32_e32 v5, v37
	v_mov_b32_e32 v37, v7
	s_waitcnt lgkmcnt(0)
	s_nop 1
	v_add_f32_dpp v6, v6, v6 row_ror:1 row_mask:0xf bank_mask:0xf
	v_mul_f32_e32 v6, 0x3a800000, v6
	v_pk_add_f32 v[38:39], v[12:13], v[6:7] op_sel_hi:[1,0] neg_lo:[0,1] neg_hi:[0,1]
	v_pk_add_f32 v[40:41], v[14:15], v[6:7] op_sel_hi:[1,0] neg_lo:[0,1] neg_hi:[0,1]
	v_pk_add_f32 v[46:47], v[4:5], v[6:7] op_sel_hi:[1,0] neg_lo:[0,1] neg_hi:[0,1]
	v_pk_add_f32 v[36:37], v[36:37], v[6:7] op_sel_hi:[1,0] neg_lo:[0,1] neg_hi:[0,1]
	v_pk_add_f32 v[42:43], v[16:17], v[6:7] op_sel_hi:[1,0] neg_lo:[0,1] neg_hi:[0,1]
	v_pk_add_f32 v[44:45], v[18:19], v[6:7] op_sel_hi:[1,0] neg_lo:[0,1] neg_hi:[0,1]
	v_pk_add_f32 v[48:49], v[8:9], v[6:7] op_sel_hi:[1,0] neg_lo:[0,1] neg_hi:[0,1]
	v_pk_add_f32 v[50:51], v[10:11], v[6:7] op_sel_hi:[1,0] neg_lo:[0,1] neg_hi:[0,1]
	v_mov_b32_e32 v6, v39
	v_mov_b32_e32 v7, v41
	v_mov_b32_e32 v14, v47
	v_mov_b32_e32 v15, v37
	v_mov_b32_e32 v4, v38
	v_mov_b32_e32 v5, v40
	v_mov_b32_e32 v12, v46
	v_mov_b32_e32 v13, v36
	v_pk_mul_f32 v[6:7], v[6:7], v[6:7]
	v_pk_mul_f32 v[14:15], v[14:15], v[14:15]
	v_mul_f32_e32 v16, v48, v48
	v_mul_f32_e32 v18, v50, v50
	v_pk_fma_f32 v[4:5], v[4:5], v[4:5], v[6:7]
	v_pk_fma_f32 v[6:7], v[12:13], v[12:13], v[14:15]
	v_pk_mul_f32 v[8:9], v[42:43], v[42:43]
	v_pk_mul_f32 v[10:11], v[44:45], v[44:45]
	v_pk_fma_f32 v[16:17], v[48:49], v[48:49], v[16:17] op_sel_hi:[1,1,0]
	v_pk_fma_f32 v[18:19], v[50:51], v[50:51], v[18:19] op_sel_hi:[1,1,0]
	v_pk_add_f32 v[4:5], v[4:5], v[4:5] op_sel_hi:[0,1]
	v_pk_add_f32 v[6:7], v[6:7], v[6:7] op_sel_hi:[0,1]
	v_mov_b32_e32 v16, v8
	v_mov_b32_e32 v18, v9
	v_mov_b32_e32 v4, v10
	v_mov_b32_e32 v6, v11
	v_pk_add_f32 v[8:9], v[16:17], v[18:19]
	v_pk_add_f32 v[4:5], v[4:5], v[6:7]
	s_nop 0
	v_pk_add_f32 v[4:5], v[8:9], v[4:5]
	s_nop 0
	v_add_f32_e32 v59, v4, v5
	global_load_dwordx4 v[4:7], v2, s[6:7] offset:2048
	global_load_dwordx4 v[8:11], v2, s[8:9] offset:2048
	global_load_dwordx4 v[12:15], v2, s[6:7] offset:3072
	global_load_dwordx4 v[16:19], v2, s[8:9] offset:3072
	ds_bpermute_b32 v53, v53, v59
	s_waitcnt lgkmcnt(0)
	v_add_f32_e32 v2, v59, v53
	ds_bpermute_b32 v53, v54, v2
	v_mov_b32_e32 v54, 0x3727c5ac
	s_waitcnt lgkmcnt(0)
	v_add_f32_e32 v2, v2, v53
	v_mov_b32_e32 v55, 0x260
	s_waitcnt lgkmcnt(0)
	s_nop 1
	v_add_f32_dpp v2, v2, v2 row_ror:8 row_mask:0xf bank_mask:0xf
	s_waitcnt lgkmcnt(0)
	s_nop 1
	v_add_f32_dpp v2, v2, v2 row_ror:4 row_mask:0xf bank_mask:0xf
	s_waitcnt lgkmcnt(0)
	s_nop 1
	v_add_f32_dpp v2, v2, v2 row_ror:2 row_mask:0xf bank_mask:0xf
	s_waitcnt lgkmcnt(0)
	s_nop 1
	v_add_f32_dpp v2, v2, v2 row_ror:1 row_mask:0xf bank_mask:0xf
	v_fmac_f32_e32 v54, 0x3a800000, v2
	v_mul_f32_e32 v2, 0x4f800000, v54
	v_cmp_gt_f32_e32 vcc, s0, v54
	s_nop 1
	v_cndmask_b32_e32 v53, v54, v2, vcc
	v_sqrt_f32_e32 v54, v53
	v_lshlrev_b32_e32 v2, 3, v52
	v_lshl_add_u64 v[0:1], v[0:1], 0, v[2:3]
	v_add_u32_e32 v52, -1, v54
	v_add_u32_e32 v56, 1, v54
	v_fma_f32 v57, -v52, v54, v53
	v_fma_f32 v58, -v56, v54, v53
	v_cmp_ge_f32_e64 s[0:1], 0, v57
	s_nop 1
	v_cndmask_b32_e64 v52, v54, v52, s[0:1]
	v_cmp_lt_f32_e64 s[0:1], 0, v58
	s_nop 1
	v_cndmask_b32_e64 v52, v52, v56, s[0:1]
	v_mul_f32_e32 v54, 0x37800000, v52
	v_cndmask_b32_e32 v52, v52, v54, vcc
	v_cmp_class_f32_e32 vcc, v53, v55
	s_nop 1
	v_cndmask_b32_e32 v52, v52, v53, vcc
	v_div_scale_f32 v53, s[0:1], v52, v52, 1.0
	v_rcp_f32_e32 v54, v53
	v_div_scale_f32 v2, vcc, 1.0, v52, 1.0
	v_fma_f32 v3, -v53, v54, 1.0
	v_fmac_f32_e32 v54, v3, v54
	v_mul_f32_e32 v3, v2, v54
	v_fma_f32 v55, -v53, v3, v2
	v_fmac_f32_e32 v3, v55, v54
	v_fma_f32 v2, -v53, v3, v2
	v_div_fmas_f32 v2, v2, v54, v3
	v_div_fixup_f32 v2, v2, v52, 1.0
	v_pk_mul_f32 v[38:39], v[38:39], v[2:3] op_sel_hi:[1,0]
	v_pk_mul_f32 v[40:41], v[40:41], v[2:3] op_sel_hi:[1,0]
	v_pk_mul_f32 v[46:47], v[46:47], v[2:3] op_sel_hi:[1,0]
	v_pk_mul_f32 v[36:37], v[36:37], v[2:3] op_sel_hi:[1,0]
	v_pk_mul_f32 v[48:49], v[48:49], v[2:3] op_sel_hi:[1,0]
	v_pk_mul_f32 v[50:51], v[50:51], v[2:3] op_sel_hi:[1,0]
	v_pk_mul_f32 v[42:43], v[42:43], v[2:3] op_sel_hi:[1,0]
	v_pk_mul_f32 v[2:3], v[44:45], v[2:3] op_sel_hi:[1,0]
	s_waitcnt vmcnt(6)
	v_pk_fma_f32 v[20:21], v[20:21], v[38:39], v[24:25]
	v_pk_fma_f32 v[22:23], v[22:23], v[40:41], v[26:27]
	s_waitcnt vmcnt(4)
	v_pk_fma_f32 v[24:25], v[28:29], v[46:47], v[32:33]
	v_pk_fma_f32 v[26:27], v[30:31], v[36:37], v[34:35]
	s_waitcnt vmcnt(2)
	v_pk_fma_f32 v[4:5], v[48:49], v[4:5], v[8:9]
	v_pk_fma_f32 v[6:7], v[50:51], v[6:7], v[10:11]
	s_waitcnt vmcnt(0)
	v_pk_fma_f32 v[8:9], v[42:43], v[12:13], v[16:17]
	v_pk_fma_f32 v[2:3], v[2:3], v[14:15], v[18:19]
	v_cvt_pk_f16_f32 v10, v20, v21
	v_cvt_pk_f16_f32 v11, v22, v23
	v_cvt_pk_f16_f32 v12, v24, v25
	v_cvt_pk_f16_f32 v13, v26, v27
	v_cvt_pk_f16_f32 v4, v4, v5
	v_cvt_pk_f16_f32 v5, v6, v7
	v_cvt_pk_f16_f32 v6, v8, v9
	v_cvt_pk_f16_f32 v7, v2, v3
	global_store_dwordx2 v[0:1], v[10:11], off
	global_store_dwordx2 v[0:1], v[12:13], off offset:512
	global_store_dwordx2 v[0:1], v[4:5], off offset:1024
	global_store_dwordx2 v[0:1], v[6:7], off offset:1536
	s_endpgm
	s_endpgm
	s_endpgm
	s_endpgm
	s_endpgm
	s_endpgm
	s_endpgm
	s_endpgm
	s_endpgm
	s_endpgm
	s_endpgm
	s_endpgm
	s_endpgm
	s_endpgm
	s_endpgm
	s_endpgm
	s_endpgm
	s_endpgm
	s_endpgm
	s_endpgm
	s_endpgm
	s_endpgm
	s_endpgm
	s_endpgm
	s_endpgm
	s_endpgm
	s_endpgm
	s_endpgm
	s_endpgm
	s_endpgm
	s_endpgm
	s_endpgm
	s_endpgm
	s_endpgm
	s_endpgm
	s_endpgm
	s_endpgm
	s_endpgm
	s_endpgm
	s_endpgm
	s_endpgm
	s_endpgm
	s_endpgm
	s_endpgm

_Z9ln_kernelILi4EEvPKiPKfS3_PfS3_S3_PDF16_:
	s_load_dwordx8 s[4:11], s[0:1], 0x8
	v_and_b32_e32 v12, 63, v0
	v_lshrrev_b32_e32 v0, 6, v0
	v_lshl_or_b32 v0, s2, 2, v0
	v_ashrrev_i32_e32 v1, 31, v0
	v_lshlrev_b64 v[24:25], 11, v[0:1]
	v_mov_b32_e32 v29, 0
	s_waitcnt lgkmcnt(0)
	v_lshl_add_u64 v[2:3], s[4:5], 0, v[24:25]
	v_lshlrev_b32_e32 v26, 3, v12
	v_mov_b32_e32 v27, v29
	v_lshl_add_u64 v[4:5], v[2:3], 0, v[26:27]
	s_mov_b64 s[2:3], 0x400000
	v_lshl_add_u64 v[10:11], v[4:5], 0, s[2:3]
	global_load_dwordx2 v[6:7], v[4:5], off offset:512
	global_load_dwordx2 v[8:9], v[4:5], off
	global_load_dwordx2 v[46:47], v[10:11], off offset:512
	s_mov_b32 s2, 0x400000
	v_add_co_u32_e32 v2, vcc, s2, v4
	v_lshlrev_b64 v[0:1], 12, v[0:1]
	s_nop 0
	v_addc_co_u32_e32 v3, vcc, 0, v5, vcc
	global_load_dwordx2 v[48:49], v[2:3], off
	v_lshl_add_u64 v[0:1], s[8:9], 0, v[0:1]
	v_lshlrev_b32_e32 v28, 4, v12
	v_lshl_add_u64 v[50:51], v[0:1], 0, v[28:29]
	global_load_dwordx4 v[0:3], v[50:51], off
	global_load_dwordx4 v[34:37], v28, s[6:7] offset:1024
	global_load_dwordx4 v[38:41], v[50:51], off offset:1024
	global_load_dwordx2 v[52:53], v[4:5], off offset:1024
	global_load_dwordx2 v[54:55], v[10:11], off offset:1024
	global_load_dwordx2 v[32:33], v[4:5], off offset:1536
	global_load_dwordx2 v[30:31], v[10:11], off offset:1536
	global_load_dwordx4 v[16:19], v[50:51], off offset:2048
	global_load_dwordx4 v[42:45], v28, s[6:7]
	global_load_dwordx4 v[20:23], v28, s[6:7] offset:2048
	global_load_dwordx4 v[12:15], v[50:51], off offset:3072
	global_load_dwordx4 v[60:63], v28, s[6:7] offset:3072
	s_load_dwordx4 s[4:7], s[0:1], 0x28
	s_mov_b32 s0, 0xf800000
	s_waitcnt lgkmcnt(0)
	v_lshl_add_u64 v[24:25], s[6:7], 0, v[24:25]
	v_lshl_add_u64 v[24:25], v[24:25], 0, v[26:27]
	s_waitcnt vmcnt(15)
	v_cvt_f32_f16_e32 v4, v6
	v_cvt_f32_f16_sdwa v5, v6 dst_sel:DWORD dst_unused:UNUSED_PAD src0_sel:WORD_1
	v_cvt_f32_f16_e32 v56, v7
	v_cvt_f32_f16_sdwa v57, v7 dst_sel:DWORD dst_unused:UNUSED_PAD src0_sel:WORD_1
	s_waitcnt vmcnt(13)
	v_cvt_f32_f16_e32 v6, v46
	v_cvt_f32_f16_sdwa v7, v46 dst_sel:DWORD dst_unused:UNUSED_PAD src0_sel:WORD_1
	v_cvt_f32_f16_e32 v58, v47
	v_cvt_f32_f16_sdwa v59, v47 dst_sel:DWORD dst_unused:UNUSED_PAD src0_sel:WORD_1
	v_cvt_f32_f16_e32 v10, v8
	v_pk_add_f32 v[50:51], v[4:5], v[6:7]
	v_add_f32_e32 v58, v56, v58
	v_add_f32_e32 v57, v57, v59
	s_waitcnt vmcnt(10)
	v_mov_b32_e32 v56, v37
	s_waitcnt vmcnt(9)
	v_pk_add_f32 v[38:39], v[38:39], v[50:51]
	v_add_f32_e32 v37, v40, v58
	v_add_f32_e32 v40, v41, v57
	s_waitcnt vmcnt(8)
	v_cvt_f32_f16_e32 v41, v52
	v_cvt_f32_f16_sdwa v50, v52 dst_sel:DWORD dst_unused:UNUSED_PAD src0_sel:WORD_1
	s_waitcnt vmcnt(7)
	v_cvt_f32_f16_e32 v52, v54
	v_cvt_f32_f16_sdwa v11, v8 dst_sel:DWORD dst_unused:UNUSED_PAD src0_sel:WORD_1
	v_cvt_f32_f16_e32 v46, v48
	v_cvt_f32_f16_sdwa v47, v48 dst_sel:DWORD dst_unused:UNUSED_PAD src0_sel:WORD_1
	v_cvt_f32_f16_e32 v8, v9
	v_cvt_f32_f16_sdwa v9, v9 dst_sel:DWORD dst_unused:UNUSED_PAD src0_sel:WORD_1
	v_cvt_f32_f16_e32 v48, v49
	v_cvt_f32_f16_sdwa v49, v49 dst_sel:DWORD dst_unused:UNUSED_PAD src0_sel:WORD_1
	v_cvt_f32_f16_e32 v51, v53
	v_cvt_f32_f16_sdwa v53, v53 dst_sel:DWORD dst_unused:UNUSED_PAD src0_sel:WORD_1
	v_pk_add_f32 v[34:35], v[34:35], v[38:39]
	v_add_f32_e32 v36, v36, v37
	v_cvt_f32_f16_sdwa v37, v54 dst_sel:DWORD dst_unused:UNUSED_PAD src0_sel:WORD_1
	v_cvt_f32_f16_e32 v38, v55
	v_cvt_f32_f16_sdwa v54, v55 dst_sel:DWORD dst_unused:UNUSED_PAD src0_sel:WORD_1
	s_waitcnt vmcnt(6)
	v_cvt_f32_f16_e32 v39, v32
	v_cvt_f32_f16_sdwa v57, v32 dst_sel:DWORD dst_unused:UNUSED_PAD src0_sel:WORD_1
	v_add_f32_e32 v32, v41, v52
	s_waitcnt vmcnt(4)
	v_add_f32_e32 v16, v16, v32
	v_pk_add_f32 v[46:47], v[10:11], v[46:47]
	s_waitcnt vmcnt(2)
	v_add_f32_e32 v32, v20, v16
	v_mbcnt_lo_u32_b32 v16, -1, 0
	v_pk_add_f32 v[48:49], v[8:9], v[48:49]
	v_pk_add_f32 v[46:47], v[0:1], v[46:47]
	v_add_f32_e32 v38, v51, v38
	v_cvt_f32_f16_e32 v51, v30
	v_cvt_f32_f16_sdwa v41, v30 dst_sel:DWORD dst_unused:UNUSED_PAD src0_sel:WORD_1
	v_add_f32_e32 v30, v53, v54
	v_mbcnt_hi_u32_b32 v54, -1, v16
	v_pk_add_f32 v[48:49], v[2:3], v[48:49]
	v_pk_add_f32 v[42:43], v[42:43], v[46:47]
	v_cvt_f32_f16_e32 v47, v33
	v_cvt_f32_f16_e32 v53, v31
	v_and_b32_e32 v16, 64, v54
	v_pk_add_f32 v[44:45], v[44:45], v[48:49]
	v_cvt_f32_f16_sdwa v49, v33 dst_sel:DWORD dst_unused:UNUSED_PAD src0_sel:WORD_1
	v_cvt_f32_f16_sdwa v31, v31 dst_sel:DWORD dst_unused:UNUSED_PAD src0_sel:WORD_1
	v_add_u32_e32 v55, 64, v16
	v_xor_b32_e32 v16, 32, v54
	v_cmp_lt_i32_e32 vcc, v16, v55
	v_add_f32_e32 v52, v50, v37
	v_add_f32_e32 v18, v18, v38
	v_cndmask_b32_e32 v16, v54, v16, vcc
	v_mov_b32_e32 v46, v17
	v_mov_b32_e32 v38, v44
	v_mov_b32_e32 v50, v45
	v_lshlrev_b32_e32 v58, 2, v16
	v_pk_add_f32 v[16:17], v[46:47], v[52:53]
	v_mov_b32_e32 v20, v21
	s_waitcnt vmcnt(1)
	v_mov_b32_e32 v21, v14
	v_mov_b32_e32 v48, v19
	v_pk_add_f32 v[38:39], v[38:39], v[50:51]
	v_pk_add_f32 v[50:51], v[42:43], v[42:43] op_sel:[0,1] op_sel_hi:[1,0]
	v_pk_add_f32 v[40:41], v[56:57], v[40:41]
	v_pk_add_f32 v[20:21], v[20:21], v[16:17]
	v_pk_add_f32 v[16:17], v[48:49], v[30:31]
	v_mov_b32_e32 v14, v23
	v_mov_b32_e32 v37, v13
	v_pk_add_f32 v[46:47], v[34:35], v[34:35] op_sel:[0,1] op_sel_hi:[1,0]
	v_mov_b32_e32 v51, v12
	v_add_f32_e32 v22, v22, v18
	v_pk_add_f32 v[30:31], v[14:15], v[16:17]
	v_pk_add_f32 v[18:19], v[36:37], v[40:41]
	s_waitcnt vmcnt(0)
	v_mov_b32_e32 v47, v61
	v_mov_b32_e32 v33, v62
	v_mov_b32_e32 v23, v63
	v_pk_add_f32 v[12:13], v[50:51], v[38:39]
	v_mov_b32_e32 v38, v29
	v_mov_b32_e32 v39, v60
	v_pk_add_f32 v[46:47], v[46:47], v[18:19]
	v_pk_add_f32 v[48:49], v[32:33], v[20:21]
	v_pk_add_f32 v[52:53], v[22:23], v[30:31]
	v_pk_add_f32 v[12:13], v[38:39], v[12:13]
	v_pk_add_f32 v[18:19], v[48:49], v[52:53]
	v_pk_add_f32 v[38:39], v[12:13], v[46:47]
	v_mov_b32_e32 v37, v40
	v_pk_add_f32 v[18:19], v[38:39], v[18:19]
	v_mov_b32_e32 v33, v20
	v_add_f32_e32 v12, v18, v19
	ds_bpermute_b32 v18, v58, v12
	v_xor_b32_e32 v19, 16, v54
	v_cmp_lt_i32_e32 vcc, v19, v55
	v_mov_b32_e32 v23, v30
	v_mov_b32_e32 v46, v13
	v_cndmask_b32_e32 v19, v54, v19, vcc
	v_lshlrev_b32_e32 v29, 2, v19
	s_waitcnt lgkmcnt(0)
	v_add_f32_e32 v12, v12, v18
	ds_bpermute_b32 v18, v29, v12
	v_xor_b32_e32 v19, 8, v54
	v_cmp_lt_i32_e32 vcc, v19, v55
	v_mov_b32_e32 v52, v49
	global_load_dwordx4 v[4:7], v28, s[10:11]
	global_load_dwordx4 v[8:11], v28, s[10:11] offset:1024
	v_cndmask_b32_e32 v19, v54, v19, vcc
	v_lshlrev_b32_e32 v48, 2, v19
	s_waitcnt lgkmcnt(0)
	v_add_f32_e32 v12, v12, v18
	v_xor_b32_e32 v19, 4, v54
	v_cmp_lt_i32_e32 vcc, v19, v55
	global_load_dwordx4 v[0:3], v28, s[10:11] offset:2048
	global_load_dwordx4 v[14:17], v28, s[10:11] offset:3072
	v_cndmask_b32_e32 v19, v54, v19, vcc
	v_lshlrev_b32_e32 v59, 2, v19
	s_waitcnt lgkmcnt(0)
	s_nop 1
	v_add_f32_dpp v12, v12, v12 row_ror:8 row_mask:0xf bank_mask:0xf
	v_xor_b32_e32 v19, 2, v54
	v_cmp_lt_i32_e32 vcc, v19, v55
	s_waitcnt lgkmcnt(0)
	s_nop 1
	v_add_f32_dpp v12, v12, v12 row_ror:4 row_mask:0xf bank_mask:0xf
	v_cndmask_b32_e32 v19, v54, v19, vcc
	v_lshlrev_b32_e32 v60, 2, v19
	v_xor_b32_e32 v19, 1, v54
	v_cmp_lt_i32_e32 vcc, v19, v55
	s_waitcnt lgkmcnt(0)
	s_nop 1
	v_add_f32_dpp v12, v12, v12 row_ror:2 row_mask:0xf bank_mask:0xf
	v_cndmask_b32_e32 v19, v54, v19, vcc
	v_lshlrev_b32_e32 v61, 2, v19
	s_waitcnt lgkmcnt(0)
	s_nop 1
	v_add_f32_dpp v12, v12, v12 row_ror:1 row_mask:0xf bank_mask:0xf
	v_mul_f32_e32 v12, 0x3a800000, v12
	v_pk_add_f32 v[42:43], v[42:43], v[12:13] op_sel_hi:[1,0] neg_lo:[0,1] neg_hi:[0,1]
	v_pk_add_f32 v[44:45], v[44:45], v[12:13] op_sel_hi:[1,0] neg_lo:[0,1] neg_hi:[0,1]
	v_mov_b32_e32 v38, v43
	v_mov_b32_e32 v39, v45
	v_pk_add_f32 v[50:51], v[34:35], v[12:13] op_sel_hi:[1,0] neg_lo:[0,1] neg_hi:[0,1]
	v_pk_add_f32 v[54:55], v[36:37], v[12:13] op_sel_hi:[1,0] neg_lo:[0,1] neg_hi:[0,1]
	v_pk_add_f32 v[56:57], v[32:33], v[12:13] op_sel_hi:[1,0] neg_lo:[0,1] neg_hi:[0,1]
	v_mov_b32_e32 v18, v42
	v_mov_b32_e32 v19, v44
	v_pk_mul_f32 v[38:39], v[38:39], v[38:39]
	v_mov_b32_e32 v34, v51
	v_mov_b32_e32 v35, v55
	v_mul_f32_e32 v30, v56, v56
	v_pk_fma_f32 v[38:39], v[18:19], v[18:19], v[38:39]
	v_mov_b32_e32 v18, v50
	v_mov_b32_e32 v19, v54
	v_pk_mul_f32 v[34:35], v[34:35], v[34:35]
	v_pk_fma_f32 v[30:31], v[56:57], v[56:57], v[30:31] op_sel_hi:[1,1,0]
	v_pk_add_f32 v[22:23], v[22:23], v[12:13] op_sel_hi:[1,0] neg_lo:[0,1] neg_hi:[0,1]
	v_pk_fma_f32 v[34:35], v[18:19], v[18:19], v[34:35]
	v_mul_f32_e32 v30, v22, v22
	v_pk_add_f32 v[46:47], v[46:47], v[12:13] op_sel_hi:[1,0] neg_lo:[0,1] neg_hi:[0,1]
	v_pk_add_f32 v[12:13], v[52:53], v[12:13] op_sel_hi:[1,0] neg_lo:[0,1] neg_hi:[0,1]
	v_pk_add_f32 v[36:37], v[38:39], v[38:39] op_sel_hi:[0,1]
	v_pk_add_f32 v[34:35], v[34:35], v[34:35] op_sel_hi:[0,1]
	v_pk_fma_f32 v[32:33], v[22:23], v[22:23], v[30:31] op_sel_hi:[1,1,0]
	v_pk_mul_f32 v[38:39], v[46:47], v[46:47]
	v_pk_mul_f32 v[40:41], v[12:13], v[12:13]
	v_mov_b32_e32 v30, v38
	v_mov_b32_e32 v32, v39
	v_mov_b32_e32 v36, v40
	v_mov_b32_e32 v34, v41
	v_pk_add_f32 v[30:31], v[30:31], v[32:33]
	v_pk_add_f32 v[32:33], v[36:37], v[34:35]
	global_load_dwordx4 v[18:21], v28, s[4:5]
	v_pk_add_f32 v[30:31], v[30:31], v[32:33]
	s_nop 0
	v_add_f32_e32 v34, v30, v31
	ds_bpermute_b32 v35, v58, v34
	global_load_dwordx4 v[30:33], v28, s[4:5] offset:1024
	s_waitcnt lgkmcnt(0)
	v_add_f32_e32 v38, v34, v35
	ds_bpermute_b32 v29, v29, v38
	global_load_dwordx4 v[34:37], v28, s[4:5] offset:2048
	s_waitcnt lgkmcnt(0)
	v_add_f32_e32 v29, v38, v29
	global_load_dwordx4 v[38:41], v28, s[4:5] offset:3072
	s_waitcnt lgkmcnt(0)
	s_nop 1
	v_add_f32_dpp v28, v29, v29 row_ror:8 row_mask:0xf bank_mask:0xf
	s_waitcnt lgkmcnt(0)
	s_nop 1
	v_add_f32_dpp v28, v28, v28 row_ror:4 row_mask:0xf bank_mask:0xf
	s_waitcnt lgkmcnt(0)
	s_nop 1
	v_add_f32_dpp v28, v28, v28 row_ror:2 row_mask:0xf bank_mask:0xf
	s_waitcnt lgkmcnt(0)
	s_nop 1
	v_add_f32_dpp v28, v28, v28 row_ror:1 row_mask:0xf bank_mask:0xf
	v_mov_b32_e32 v29, 0x3727c5ac
	v_fmac_f32_e32 v29, 0x3a800000, v28
	v_mul_f32_e32 v28, 0x4f800000, v29
	v_cmp_gt_f32_e32 vcc, s0, v29
	s_nop 1
	v_cndmask_b32_e32 v28, v29, v28, vcc
	v_sqrt_f32_e32 v29, v28
	s_nop 0
	v_add_u32_e32 v48, -1, v29
	v_fma_f32 v49, -v48, v29, v28
	v_cmp_ge_f32_e64 s[0:1], 0, v49
	v_add_u32_e32 v49, 1, v29
	s_nop 0
	v_cndmask_b32_e64 v48, v29, v48, s[0:1]
	v_fma_f32 v29, -v49, v29, v28
	v_cmp_lt_f32_e64 s[0:1], 0, v29
	s_nop 1
	v_cndmask_b32_e64 v29, v48, v49, s[0:1]
	v_mul_f32_e32 v48, 0x37800000, v29
	v_cndmask_b32_e32 v29, v29, v48, vcc
	v_mov_b32_e32 v48, 0x260
	v_cmp_class_f32_e32 vcc, v28, v48
	s_nop 1
	v_cndmask_b32_e32 v28, v29, v28, vcc
	v_div_scale_f32 v29, s[0:1], v28, v28, 1.0
	v_rcp_f32_e32 v48, v29
	s_nop 0
	v_fma_f32 v26, -v29, v48, 1.0
	v_fmac_f32_e32 v48, v26, v48
	v_div_scale_f32 v26, vcc, 1.0, v28, 1.0
	v_mul_f32_e32 v27, v26, v48
	v_fma_f32 v49, -v29, v27, v26
	v_fmac_f32_e32 v27, v49, v48
	v_fma_f32 v26, -v29, v27, v26
	v_div_fmas_f32 v26, v26, v48, v27
	v_div_fixup_f32 v26, v26, v28, 1.0
	v_pk_mul_f32 v[28:29], v[42:43], v[26:27] op_sel_hi:[1,0]
	s_waitcnt vmcnt(3)
	v_pk_fma_f32 v[4:5], v[4:5], v[28:29], v[18:19]
	v_pk_mul_f32 v[18:19], v[44:45], v[26:27] op_sel_hi:[1,0]
	v_cvt_pk_f16_f32 v4, v4, v5
	v_pk_fma_f32 v[6:7], v[6:7], v[18:19], v[20:21]
	s_nop 0
	v_cvt_pk_f16_f32 v5, v6, v7
	global_store_dwordx2 v[24:25], v[4:5], off
	v_pk_mul_f32 v[4:5], v[50:51], v[26:27] op_sel_hi:[1,0]
	v_pk_mul_f32 v[6:7], v[54:55], v[26:27] op_sel_hi:[1,0]
	s_waitcnt vmcnt(3)
	v_pk_fma_f32 v[4:5], v[8:9], v[4:5], v[30:31]
	v_pk_fma_f32 v[6:7], v[10:11], v[6:7], v[32:33]
	v_cvt_pk_f16_f32 v4, v4, v5
	v_cvt_pk_f16_f32 v5, v6, v7
	global_store_dwordx2 v[24:25], v[4:5], off offset:512
	v_pk_mul_f32 v[4:5], v[56:57], v[26:27] op_sel_hi:[1,0]
	s_waitcnt vmcnt(3)
	v_pk_fma_f32 v[0:1], v[0:1], v[4:5], v[34:35]
	v_pk_mul_f32 v[4:5], v[22:23], v[26:27] op_sel_hi:[1,0]
	v_cvt_pk_f16_f32 v0, v0, v1
	v_pk_fma_f32 v[2:3], v[4:5], v[2:3], v[36:37]
	s_nop 0
	v_cvt_pk_f16_f32 v1, v2, v3
	global_store_dwordx2 v[24:25], v[0:1], off offset:1024
	v_pk_mul_f32 v[0:1], v[46:47], v[26:27] op_sel_hi:[1,0]
	v_pk_mul_f32 v[2:3], v[12:13], v[26:27] op_sel_hi:[1,0]
	s_waitcnt vmcnt(3)
	v_pk_fma_f32 v[0:1], v[0:1], v[14:15], v[38:39]
	v_pk_fma_f32 v[2:3], v[2:3], v[16:17], v[40:41]
	v_cvt_pk_f16_f32 v0, v0, v1
	v_cvt_pk_f16_f32 v1, v2, v3
	global_store_dwordx2 v[24:25], v[0:1], off offset:1536
	s_endpgm
	s_endpgm
	s_endpgm
	s_endpgm
	s_endpgm
	s_endpgm
	s_endpgm
	s_endpgm
	s_endpgm
	s_endpgm
	s_endpgm
	s_endpgm
	s_endpgm
	s_endpgm
	s_endpgm
	s_endpgm
	s_endpgm
	s_endpgm
	s_endpgm
	s_endpgm
	s_endpgm
	s_endpgm
	s_endpgm
